# E36: E35 + combine phase forget-logit weight LDS reads issued 4 ahead into spare VGPRs (software pipelining of ds_read_b128)
# speedup vs baseline: 1.0168x; 1.0002x over previous
.LBB0_1864:
	v_mul_f32_e32 v73, v124, v124
	v_mul_f32_e32 v100, v126, v126
	v_fmac_f32_e32 v73, v125, v125
	v_fmac_f32_e32 v100, v127, v127
	v_add_f32_e32 v73, v100, v73
	v_mul_f32_e32 v100, v128, v128
	v_mul_f32_e32 v140, v130, v130
	v_fmac_f32_e32 v100, v129, v129
	v_fmac_f32_e32 v140, v131, v131
	v_add_f32_e32 v100, v140, v100
	v_add_f32_e32 v73, v100, v73
	v_mul_f32_e32 v100, v132, v132
	v_mul_f32_e32 v140, v134, v134
	v_fmac_f32_e32 v100, v133, v133
	v_fmac_f32_e32 v140, v135, v135
	v_add_f32_e32 v100, v140, v100
	v_add_f32_e32 v73, v100, v73
	v_mul_f32_e32 v100, v136, v136
	v_mul_f32_e32 v140, v138, v138
	v_fmac_f32_e32 v100, v137, v137
	v_fmac_f32_e32 v140, v139, v139
	v_add_f32_e32 v100, v140, v100
	v_add_f32_e32 v73, v100, v73
	s_nop 1
	v_add_f32_dpp v73, v73, v73 quad_perm:[1,0,3,2] row_mask:0xf bank_mask:0xf bound_ctrl:1
	s_nop 1
	v_add_f32_dpp v73, v73, v73 quad_perm:[2,3,0,1] row_mask:0xf bank_mask:0xf bound_ctrl:1
	s_nop 1
	v_add_f32_dpp v73, v73, v73 row_half_mirror row_mask:0xf bank_mask:0xf bound_ctrl:1
	s_nop 1
	v_add_f32_dpp v73, v73, v73 row_mirror row_mask:0xf bank_mask:0xf bound_ctrl:1
	v_mov_b32_e32 v100, v73
	s_nop 1
	v_permlane16_swap_b32_e32 v73, v100
	v_add_f32_e32 v73, v73, v100
	v_mov_b32_e32 v100, v73
	s_nop 1
	v_permlane32_swap_b32_e32 v73, v100
	v_add_f32_e32 v73, v73, v100
	v_fmamk_f32 v73, v73, 0x3a800000, v215
	v_mul_f32_e32 v100, 0x4f800000, v73
	v_cmp_gt_f32_e32 vcc, s59, v73
	s_nop 1
	v_cndmask_b32_e32 v73, v73, v100, vcc
	v_sqrt_f32_e32 v100, v73
	s_nop 0
	v_add_u32_e32 v140, -1, v100
	v_fma_f32 v141, -v140, v100, v73
	v_cmp_ge_f32_e64 s[4:5], 0, v141
	v_add_u32_e32 v141, 1, v100
	s_nop 0
	v_cndmask_b32_e64 v140, v100, v140, s[4:5]
	v_fma_f32 v100, -v141, v100, v73
	v_cmp_lt_f32_e64 s[4:5], 0, v100
	s_nop 1
	v_cndmask_b32_e64 v100, v140, v141, s[4:5]
	v_mul_f32_e32 v140, 0x37800000, v100
	v_cndmask_b32_e32 v100, v100, v140, vcc
	v_cmp_class_f32_e32 vcc, v73, v212
	s_nop 1
	v_cndmask_b32_e32 v73, v100, v73, vcc
	v_div_scale_f32 v100, s[4:5], v73, v73, 1.0
	v_rcp_f32_e32 v140, v100
	s_mov_b64 s[4:5], -1
	v_fma_f32 v141, -v100, v140, 1.0
	v_fmac_f32_e32 v140, v141, v140
	v_div_scale_f32 v141, vcc, 1.0, v73, 1.0
	v_mul_f32_e32 v144, v141, v140
	v_fma_f32 v145, -v100, v144, v141
	v_fmac_f32_e32 v144, v145, v140
	v_fma_f32 v100, -v100, v144, v141
	v_div_fmas_f32 v100, v100, v140, v144
	v_div_fixup_f32 v140, v100, v73, 1.0
	v_mov_b32_e32 v141, v140
	s_and_b64 vcc, exec, s[0:1]
	s_cbranch_vccnz .LBB0_1868
	v_mov_b32_e32 v144, v140
	v_mov_b32_e32 v145, v140
	v_pk_mul_f32 v[146:147], v[126:127], v[144:145]
	v_pk_mul_f32 v[148:149], v[124:125], v[140:141]
	v_pk_fma_f32 v[162:163], v[48:49], v[146:147], v[36:37]
	v_pk_fma_f32 v[164:165], v[46:47], v[148:149], v[34:35]
	ds_read_b128 v[176:179], v1
	ds_read_b128 v[180:183], v1 offset:16
	ds_read_b128 v[184:187], v1 offset:32
	ds_read_b128 v[188:191], v1 offset:48
	ds_read_b128 v[192:195], v1 offset:64
	s_mov_b32 s4, 0x37000000
	v_add_co_u32_e32 v142, vcc, s4, v142
	v_cvt_pk_bf16_f32 v150, v164, v165
	v_cvt_pk_bf16_f32 v151, v162, v163
	v_addc_co_u32_e32 v143, vcc, 0, v143, vcc
	global_store_dwordx2 v[142:143], v[150:151], off
	ds_read_b128 v[196:199], v1 offset:80
	ds_read_b128 v[200:203], v1 offset:96
	ds_read_b128 v[204:207], v1 offset:112
	s_waitcnt lgkmcnt(7)
	v_fma_f32 v73, v164, v176, 0
	v_fma_f32 v100, v164, v177, 0
	v_fma_f32 v166, v164, v178, 0
	v_fma_f32 v167, v164, v179, 0
	ds_read_b128 v[176:179], v67
	s_waitcnt lgkmcnt(7)
	v_fma_f32 v168, v164, v180, 0
	v_fma_f32 v169, v164, v181, 0
	v_fma_f32 v170, v164, v182, 0
	v_fma_f32 v171, v164, v183, 0
	ds_read_b128 v[180:183], v67 offset:16
	s_waitcnt lgkmcnt(7)
	v_fmac_f32_e32 v73, v165, v184
	v_fmac_f32_e32 v100, v165, v185
	v_fmac_f32_e32 v166, v165, v186
	v_fmac_f32_e32 v167, v165, v187
	s_waitcnt lgkmcnt(5)
	v_fmac_f32_e32 v73, v162, v192
	v_fmac_f32_e32 v100, v162, v193
	v_fmac_f32_e32 v166, v162, v194
	v_fmac_f32_e32 v167, v162, v195
	ds_read_b128 v[184:187], v1 offset:9248
	v_fmac_f32_e32 v168, v165, v188
	v_fmac_f32_e32 v169, v165, v189
	v_fmac_f32_e32 v170, v165, v190
	v_fmac_f32_e32 v171, v165, v191
	s_waitcnt lgkmcnt(5)
	v_fmac_f32_e32 v168, v162, v196
	v_fmac_f32_e32 v169, v162, v197
	v_fmac_f32_e32 v170, v162, v198
	v_fmac_f32_e32 v171, v162, v199
	ds_read_b128 v[188:191], v1 offset:9264
	s_waitcnt lgkmcnt(5)
	v_fmac_f32_e32 v73, v163, v200
	v_fmac_f32_e32 v100, v163, v201
	v_fmac_f32_e32 v166, v163, v202
	v_fmac_f32_e32 v167, v163, v203
	v_pk_mul_f32 v[146:147], v[130:131], v[144:145]
	v_pk_mul_f32 v[148:149], v[128:129], v[140:141]
	v_pk_fma_f32 v[154:155], v[44:45], v[146:147], v[28:29]
	v_pk_fma_f32 v[156:157], v[42:43], v[148:149], v[26:27]
	ds_read_b128 v[192:195], v1 offset:9280
	s_waitcnt lgkmcnt(5)
	v_fmac_f32_e32 v168, v163, v204
	v_fmac_f32_e32 v169, v163, v205
	v_cvt_pk_bf16_f32 v150, v156, v157
	v_cvt_pk_bf16_f32 v151, v154, v155
	v_fmac_f32_e32 v170, v163, v206
	v_fmac_f32_e32 v171, v163, v207
	global_store_dwordx2 v[142:143], v[150:151], off offset:512
	ds_read_b128 v[196:199], v1 offset:9296
	s_waitcnt lgkmcnt(5)
	v_fmac_f32_e32 v73, v156, v176
	v_fmac_f32_e32 v100, v156, v177
	v_fmac_f32_e32 v166, v156, v178
	v_fmac_f32_e32 v167, v156, v179
	ds_read_b128 v[200:203], v1 offset:9312
	s_waitcnt lgkmcnt(5)
	v_fmac_f32_e32 v168, v156, v180
	v_fmac_f32_e32 v169, v156, v181
	v_fmac_f32_e32 v170, v156, v182
	v_fmac_f32_e32 v171, v156, v183
	ds_read_b128 v[204:207], v1 offset:9328
	s_waitcnt lgkmcnt(5)
	v_fmac_f32_e32 v73, v157, v184
	v_fmac_f32_e32 v100, v157, v185
	v_fmac_f32_e32 v166, v157, v186
	v_fmac_f32_e32 v167, v157, v187
	ds_read_b128 v[176:179], v69
	s_waitcnt lgkmcnt(5)
	v_fmac_f32_e32 v168, v157, v188
	v_fmac_f32_e32 v169, v157, v189
	v_fmac_f32_e32 v170, v157, v190
	v_fmac_f32_e32 v171, v157, v191
	ds_read_b128 v[180:183], v69 offset:16
	s_waitcnt lgkmcnt(5)
	v_fmac_f32_e32 v73, v154, v192
	v_fmac_f32_e32 v100, v154, v193
	v_fmac_f32_e32 v166, v154, v194
	v_fmac_f32_e32 v167, v154, v195
	ds_read_b128 v[184:187], v1 offset:18464
	s_waitcnt lgkmcnt(5)
	v_fmac_f32_e32 v168, v154, v196
	v_fmac_f32_e32 v169, v154, v197
	v_fmac_f32_e32 v170, v154, v198
	v_fmac_f32_e32 v171, v154, v199
	ds_read_b128 v[188:191], v1 offset:18480
	s_waitcnt lgkmcnt(5)
	v_fmac_f32_e32 v73, v155, v200
	v_fmac_f32_e32 v100, v155, v201
	v_fmac_f32_e32 v166, v155, v202
	v_fmac_f32_e32 v167, v155, v203
	v_pk_mul_f32 v[146:147], v[134:135], v[144:145]
	v_pk_mul_f32 v[148:149], v[132:133], v[140:141]
	v_pk_fma_f32 v[162:163], v[40:41], v[146:147], v[24:25]
	v_pk_fma_f32 v[164:165], v[38:39], v[148:149], v[22:23]
	ds_read_b128 v[192:195], v1 offset:18496
	s_waitcnt lgkmcnt(5)
	v_fmac_f32_e32 v168, v155, v204
	v_fmac_f32_e32 v169, v155, v205
	v_cvt_pk_bf16_f32 v150, v164, v165
	v_cvt_pk_bf16_f32 v151, v162, v163
	v_fmac_f32_e32 v170, v155, v206
	v_fmac_f32_e32 v171, v155, v207
	global_store_dwordx2 v[142:143], v[150:151], off offset:1024
	ds_read_b128 v[196:199], v1 offset:18512
	s_waitcnt lgkmcnt(5)
	v_fmac_f32_e32 v73, v164, v176
	v_fmac_f32_e32 v100, v164, v177
	v_fmac_f32_e32 v166, v164, v178
	v_fmac_f32_e32 v167, v164, v179
	ds_read_b128 v[200:203], v1 offset:18528
	s_waitcnt lgkmcnt(5)
	v_fmac_f32_e32 v168, v164, v180
	v_fmac_f32_e32 v169, v164, v181
	v_fmac_f32_e32 v170, v164, v182
	v_fmac_f32_e32 v171, v164, v183
	ds_read_b128 v[204:207], v1 offset:18544
	ds_read_b128 v[176:179], v71
	ds_read_b128 v[180:183], v71 offset:16
	s_waitcnt lgkmcnt(7)
	v_fmac_f32_e32 v73, v165, v184
	v_fmac_f32_e32 v100, v165, v185
	v_fmac_f32_e32 v166, v165, v186
	v_fmac_f32_e32 v167, v165, v187
	ds_read_b128 v[184:187], v1 offset:27680
	s_waitcnt lgkmcnt(7)
	v_fmac_f32_e32 v168, v165, v188
	v_fmac_f32_e32 v169, v165, v189
	v_fmac_f32_e32 v170, v165, v190
	v_fmac_f32_e32 v171, v165, v191
	ds_read_b128 v[188:191], v1 offset:27696
	s_waitcnt lgkmcnt(7)
	v_fmac_f32_e32 v73, v162, v192
	v_fmac_f32_e32 v100, v162, v193
	s_waitcnt lgkmcnt(6)
	v_fmac_f32_e32 v170, v162, v198
	v_fmac_f32_e32 v171, v162, v199
	s_waitcnt lgkmcnt(5)
	v_fmac_f32_e32 v73, v163, v200
	v_fmac_f32_e32 v100, v163, v201
	v_pk_mul_f32 v[144:145], v[138:139], v[144:145]
	v_pk_mul_f32 v[146:147], v[136:137], v[140:141]
	s_waitcnt lgkmcnt(4)
	v_fmac_f32_e32 v170, v163, v206
	v_fmac_f32_e32 v171, v163, v207
	v_pk_fma_f32 v[152:153], v[32:33], v[144:145], v[20:21]
	v_pk_fma_f32 v[154:155], v[30:31], v[146:147], v[18:19]
	v_fmac_f32_e32 v166, v162, v194
	v_fmac_f32_e32 v167, v162, v195
	ds_read_b128 v[192:195], v1 offset:27712
	v_fmac_f32_e32 v168, v162, v196
	v_fmac_f32_e32 v169, v162, v197
	v_fmac_f32_e32 v166, v163, v202
	v_fmac_f32_e32 v167, v163, v203
	v_cvt_pk_bf16_f32 v148, v154, v155
	v_cvt_pk_bf16_f32 v149, v152, v153
	v_fmac_f32_e32 v168, v163, v204
	v_fmac_f32_e32 v169, v163, v205
	global_store_dwordx2 v[142:143], v[148:149], off offset:1536
	ds_read_b128 v[196:199], v1 offset:27728
	s_waitcnt lgkmcnt(5)
	v_fmac_f32_e32 v73, v154, v176
	v_fmac_f32_e32 v100, v154, v177
	ds_read_b128 v[200:203], v1 offset:27744
	v_fmac_f32_e32 v166, v154, v178
	v_fmac_f32_e32 v167, v154, v179
	s_waitcnt lgkmcnt(5)
	v_fmac_f32_e32 v168, v154, v180
	v_fmac_f32_e32 v169, v154, v181
	ds_read_b128 v[204:207], v1 offset:27760
	s_waitcnt lgkmcnt(5)
	v_fmac_f32_e32 v73, v155, v184
	v_fmac_f32_e32 v100, v155, v185
	v_fmac_f32_e32 v166, v155, v186
	v_fmac_f32_e32 v167, v155, v187
	v_fmac_f32_e32 v170, v154, v182
	v_fmac_f32_e32 v171, v154, v183
	s_waitcnt lgkmcnt(4)
	v_fmac_f32_e32 v168, v155, v188
	v_fmac_f32_e32 v169, v155, v189
	v_fmac_f32_e32 v170, v155, v190
	v_fmac_f32_e32 v171, v155, v191
	s_waitcnt lgkmcnt(3)
	v_fmac_f32_e32 v73, v152, v192
	v_fmac_f32_e32 v100, v152, v193
	v_fmac_f32_e32 v166, v152, v194
	v_fmac_f32_e32 v167, v152, v195
	s_waitcnt lgkmcnt(2)
	v_fmac_f32_e32 v168, v152, v196
	v_fmac_f32_e32 v169, v152, v197
	v_fmac_f32_e32 v170, v152, v198
	v_fmac_f32_e32 v171, v152, v199
	s_waitcnt lgkmcnt(1)
	v_fmac_f32_e32 v73, v153, v200
	v_fmac_f32_e32 v100, v153, v201
	v_fmac_f32_e32 v166, v153, v202
	v_add_f32_dpp v73, v73, v73 quad_perm:[1,0,3,2] row_mask:0xf bank_mask:0xf bound_ctrl:1
	v_fmac_f32_e32 v167, v153, v203
	s_waitcnt lgkmcnt(0)
	v_fmac_f32_e32 v168, v153, v204
	v_add_f32_dpp v73, v73, v73 quad_perm:[2,3,0,1] row_mask:0xf bank_mask:0xf bound_ctrl:1
	v_fmac_f32_e32 v169, v153, v205
	v_fmac_f32_e32 v170, v153, v206
	v_add_f32_dpp v73, v73, v73 row_half_mirror row_mask:0xf bank_mask:0xf bound_ctrl:1
	v_fmac_f32_e32 v171, v153, v207
	s_nop 0
	v_add_f32_dpp v73, v73, v73 row_mirror row_mask:0xf bank_mask:0xf bound_ctrl:1
	v_mov_b32_e32 v142, v73
	s_nop 1
	v_permlane16_swap_b32_e32 v73, v142
	v_add_f32_e32 v142, v73, v142
	s_nop 0
	v_add_f32_dpp v73, v100, v100 quad_perm:[1,0,3,2] row_mask:0xf bank_mask:0xf bound_ctrl:1
	v_mov_b32_e32 v144, v142
	s_nop 1
	v_permlane32_swap_b32_e32 v142, v144
	v_add_f32_dpp v73, v73, v73 quad_perm:[2,3,0,1] row_mask:0xf bank_mask:0xf bound_ctrl:1
	s_nop 1
	v_add_f32_dpp v73, v73, v73 row_half_mirror row_mask:0xf bank_mask:0xf bound_ctrl:1
	s_nop 1
	v_add_f32_dpp v73, v73, v73 row_mirror row_mask:0xf bank_mask:0xf bound_ctrl:1
	v_mov_b32_e32 v100, v73
	s_nop 1
	v_permlane16_swap_b32_e32 v73, v100
	v_add_f32_e32 v143, v73, v100
	s_nop 0
	v_add_f32_dpp v73, v166, v166 quad_perm:[1,0,3,2] row_mask:0xf bank_mask:0xf bound_ctrl:1
	v_mov_b32_e32 v145, v143
	s_nop 1
	v_permlane32_swap_b32_e32 v143, v145
	v_add_f32_dpp v73, v73, v73 quad_perm:[2,3,0,1] row_mask:0xf bank_mask:0xf bound_ctrl:1
	s_nop 1
	v_add_f32_dpp v73, v73, v73 row_half_mirror row_mask:0xf bank_mask:0xf bound_ctrl:1
	s_nop 1
	v_add_f32_dpp v73, v73, v73 row_mirror row_mask:0xf bank_mask:0xf bound_ctrl:1
	v_mov_b32_e32 v100, v73
	s_nop 1
	v_permlane16_swap_b32_e32 v73, v100
	v_add_f32_e32 v146, v73, v100
	s_nop 0
	v_add_f32_dpp v73, v167, v167 quad_perm:[1,0,3,2] row_mask:0xf bank_mask:0xf bound_ctrl:1
	v_mov_b32_e32 v148, v146
	s_nop 1
	v_permlane32_swap_b32_e32 v146, v148
	v_add_f32_dpp v73, v73, v73 quad_perm:[2,3,0,1] row_mask:0xf bank_mask:0xf bound_ctrl:1
	s_nop 1
	v_add_f32_dpp v73, v73, v73 row_half_mirror row_mask:0xf bank_mask:0xf bound_ctrl:1
	s_nop 1
	v_add_f32_dpp v73, v73, v73 row_mirror row_mask:0xf bank_mask:0xf bound_ctrl:1
	v_mov_b32_e32 v100, v73
	s_nop 1
	v_permlane16_swap_b32_e32 v73, v100
	v_add_f32_e32 v147, v73, v100
	s_nop 0
	v_add_f32_dpp v73, v168, v168 quad_perm:[1,0,3,2] row_mask:0xf bank_mask:0xf bound_ctrl:1
	v_mov_b32_e32 v149, v147
	s_nop 1
	v_permlane32_swap_b32_e32 v147, v149
	v_add_f32_dpp v73, v73, v73 quad_perm:[2,3,0,1] row_mask:0xf bank_mask:0xf bound_ctrl:1
	s_nop 1
	v_add_f32_dpp v73, v73, v73 row_half_mirror row_mask:0xf bank_mask:0xf bound_ctrl:1
	s_nop 1
	v_add_f32_dpp v73, v73, v73 row_mirror row_mask:0xf bank_mask:0xf bound_ctrl:1
	v_mov_b32_e32 v100, v73
	s_nop 1
	v_permlane16_swap_b32_e32 v73, v100
	v_add_f32_e32 v150, v73, v100
	s_nop 0
	v_add_f32_dpp v73, v169, v169 quad_perm:[1,0,3,2] row_mask:0xf bank_mask:0xf bound_ctrl:1
	v_mov_b32_e32 v152, v150
	s_nop 1
	v_permlane32_swap_b32_e32 v150, v152
	v_add_f32_dpp v73, v73, v73 quad_perm:[2,3,0,1] row_mask:0xf bank_mask:0xf bound_ctrl:1
	s_nop 1
	v_add_f32_dpp v73, v73, v73 row_half_mirror row_mask:0xf bank_mask:0xf bound_ctrl:1
	s_nop 1
	v_add_f32_dpp v73, v73, v73 row_mirror row_mask:0xf bank_mask:0xf bound_ctrl:1
	v_mov_b32_e32 v100, v73
	s_nop 1
	v_permlane16_swap_b32_e32 v73, v100
	v_add_f32_e32 v151, v73, v100
	s_nop 0
	v_add_f32_dpp v73, v170, v170 quad_perm:[1,0,3,2] row_mask:0xf bank_mask:0xf bound_ctrl:1
	v_mov_b32_e32 v153, v151
	s_nop 1
	v_permlane32_swap_b32_e32 v151, v153
	v_add_f32_dpp v73, v73, v73 quad_perm:[2,3,0,1] row_mask:0xf bank_mask:0xf bound_ctrl:1
	s_nop 1
	v_add_f32_dpp v73, v73, v73 row_half_mirror row_mask:0xf bank_mask:0xf bound_ctrl:1
	s_nop 1
	v_add_f32_dpp v73, v73, v73 row_mirror row_mask:0xf bank_mask:0xf bound_ctrl:1
	v_mov_b32_e32 v100, v73
	s_nop 1
	v_permlane16_swap_b32_e32 v73, v100
	v_add_f32_e32 v154, v73, v100
	s_nop 0
	v_add_f32_dpp v73, v171, v171 quad_perm:[1,0,3,2] row_mask:0xf bank_mask:0xf bound_ctrl:1
	v_mov_b32_e32 v156, v154
	s_nop 1
	v_permlane32_swap_b32_e32 v154, v156
	v_add_f32_dpp v73, v73, v73 quad_perm:[2,3,0,1] row_mask:0xf bank_mask:0xf bound_ctrl:1
	s_nop 1
	v_add_f32_dpp v73, v73, v73 row_half_mirror row_mask:0xf bank_mask:0xf bound_ctrl:1
	s_nop 1
	v_add_f32_dpp v73, v73, v73 row_mirror row_mask:0xf bank_mask:0xf bound_ctrl:1
	v_mov_b32_e32 v100, v73
	s_nop 1
	v_permlane16_swap_b32_e32 v73, v100
	v_add_f32_e32 v155, v73, v100
	v_mov_b32_e32 v157, v155
	s_nop 1
	v_permlane32_swap_b32_e32 v155, v157
	s_and_saveexec_b64 s[4:5], s[2:3]
	s_cbranch_execz .LBB0_1867
	s_add_u32 s18, s6, s12
	v_pk_add_f32 v[146:147], v[146:147], v[148:149]
	v_pk_add_f32 v[144:145], v[142:143], v[144:145]
	s_addc_u32 s19, s7, s13
	v_pk_add_f32 v[154:155], v[154:155], v[156:157]
	v_pk_add_f32 v[152:153], v[150:151], v[152:153]
	global_store_dwordx4 v213, v[144:147], s[18:19]
	global_store_dwordx4 v213, v[152:155], s[18:19] offset:16
